# mix and xo residual-add epilogues: second row half's 8 x loads issued with the first half's (one exposed load latency per tile)
# speedup vs baseline: 1.0077x; 1.0048x over previous
.LBB0_1094:
	s_lshl_b32 s10, s67, 8
	s_add_i32 s26, s10, s56
	s_lshl_b32 s10, s28, 8
	s_or_b32 s30, s10, s60
	v_or_b32_e32 v172, s26, v165
	s_ashr_i32 s31, s30, 31
	s_lshl_b32 s10, s28, 2
	s_lshl_b64 s[28:29], s[30:31], 1
	v_ashrrev_i32_e32 v173, 31, v172
	v_lshl_add_u64 v[174:175], v[170:171], 0, s[28:29]
	v_lshlrev_b64 v[120:121], 11, v[172:173]
	v_lshl_add_u64 v[120:121], v[174:175], 0, v[120:121]
	global_load_dwordx4 v[180:183], v[120:121], off
	global_load_dwordx4 v[184:187], v[120:121], off offset:64
	v_or_b32_e32 v120, 16, v172
	v_ashrrev_i32_e32 v121, 31, v120
	v_lshlrev_b64 v[120:121], 11, v[120:121]
	v_lshl_add_u64 v[120:121], v[174:175], 0, v[120:121]
	global_load_dwordx4 v[148:151], v[120:121], off
	global_load_dwordx4 v[144:147], v[120:121], off offset:64
	v_or_b32_e32 v120, 32, v172
	v_ashrrev_i32_e32 v121, 31, v120
	v_lshlrev_b64 v[120:121], 11, v[120:121]
	v_lshl_add_u64 v[120:121], v[174:175], 0, v[120:121]
	global_load_dwordx4 v[140:143], v[120:121], off
	global_load_dwordx4 v[136:139], v[120:121], off offset:64
	v_or_b32_e32 v120, 48, v172
	v_ashrrev_i32_e32 v121, 31, v120
	v_lshlrev_b64 v[120:121], 11, v[120:121]
	v_lshl_add_u64 v[120:121], v[174:175], 0, v[120:121]
	global_load_dwordx4 v[128:131], v[120:121], off
	s_nop 0
	global_load_dwordx4 v[120:123], v[120:121], off offset:64
	v_add_u32_e32 v214, 0x80, v172
	v_ashrrev_i32_e32 v215, 31, v214
	v_lshlrev_b64 v[214:215], 11, v[214:215]
	v_lshl_add_u64 v[214:215], v[174:175], 0, v[214:215]
	global_load_dwordx4 v[192:195], v[214:215], off
	global_load_dwordx4 v[196:199], v[214:215], off offset:64
	v_add_u32_e32 v214, 0x90, v172
	v_ashrrev_i32_e32 v215, 31, v214
	v_lshlrev_b64 v[214:215], 11, v[214:215]
	v_lshl_add_u64 v[214:215], v[174:175], 0, v[214:215]
	global_load_dwordx4 v[200:203], v[214:215], off
	global_load_dwordx4 v[204:207], v[214:215], off offset:64
	v_add_u32_e32 v214, 0xa0, v172
	v_ashrrev_i32_e32 v215, 31, v214
	v_lshlrev_b64 v[214:215], 11, v[214:215]
	v_lshl_add_u64 v[214:215], v[174:175], 0, v[214:215]
	global_load_dwordx4 v[232:235], v[214:215], off
	global_load_dwordx4 v[236:239], v[214:215], off offset:64
	v_add_u32_e32 v214, 0xb0, v172
	v_ashrrev_i32_e32 v215, 31, v214
	v_lshlrev_b64 v[214:215], 11, v[214:215]
	v_lshl_add_u64 v[214:215], v[174:175], 0, v[214:215]
	global_load_dwordx4 v[240:243], v[214:215], off
	global_load_dwordx4 v[244:247], v[214:215], off offset:64
	v_and_b32_e32 v177, 64, v225
	v_xor_b32_e32 v176, 8, v225
	v_add_u32_e32 v177, 64, v177
	v_cmp_lt_i32_e32 vcc, v176, v177
	v_xor_b32_e32 v179, 32, v225
	s_ashr_i32 s27, s26, 31
	v_cndmask_b32_e32 v176, v225, v176, vcc
	v_lshlrev_b32_e32 v178, 2, v176
	v_xor_b32_e32 v176, 16, v225
	v_cmp_lt_i32_e32 vcc, v176, v177
	s_ashr_i32 s11, s10, 31
	s_lshl_b64 s[30:31], s[26:27], 11
	v_cndmask_b32_e32 v176, v225, v176, vcc
	v_cmp_lt_i32_e32 vcc, v179, v177
	s_add_u32 s25, s18, s30
	s_addc_u32 s27, s19, s31
	v_cndmask_b32_e32 v177, v225, v179, vcc
	s_add_u32 s30, s25, s28
	s_addc_u32 s31, s27, s29
	v_lshlrev_b32_e32 v208, 1, v166
	s_movk_i32 s25, 0x4000
	v_lshlrev_b32_e32 v176, 2, v176
	v_lshlrev_b32_e32 v177, 2, v177
	s_waitcnt vmcnt(8)
	v_lshlrev_b32_e32 v188, 16, v180
	v_and_b32_e32 v189, 0xffff0000, v180
	v_pk_add_f32 v[132:133], v[132:133], v[188:189]
	s_nop 0
	v_cvt_pk_bf16_f32 v179, v132, v133
	v_lshlrev_b32_e32 v132, 16, v181
	v_and_b32_e32 v133, 0xffff0000, v181
	v_pk_add_f32 v[132:133], v[134:135], v[132:133]
	s_nop 0
	v_cvt_pk_bf16_f32 v134, v132, v133
	v_lshlrev_b32_e32 v132, 16, v182
	v_and_b32_e32 v133, 0xffff0000, v182
	v_pk_add_f32 v[124:125], v[124:125], v[132:133]
	s_nop 0
	v_cvt_pk_bf16_f32 v132, v124, v125
	v_lshlrev_b32_e32 v124, 16, v183
	v_and_b32_e32 v125, 0xffff0000, v183
	v_pk_add_f32 v[124:125], v[126:127], v[124:125]
	s_nop 0
	v_cvt_pk_bf16_f32 v126, v124, v125
	v_lshlrev_b32_e32 v124, 16, v184
	v_and_b32_e32 v125, 0xffff0000, v184
	v_pk_add_f32 v[116:117], v[116:117], v[124:125]
	s_nop 0
	v_cvt_pk_bf16_f32 v127, v116, v117
	v_lshlrev_b32_e32 v116, 16, v185
	v_and_b32_e32 v117, 0xffff0000, v185
	v_pk_add_f32 v[116:117], v[118:119], v[116:117]
	s_nop 0
	v_cvt_pk_bf16_f32 v133, v116, v117
	v_lshlrev_b32_e32 v116, 16, v186
	v_and_b32_e32 v117, 0xffff0000, v186
	v_pk_add_f32 v[112:113], v[112:113], v[116:117]
	s_nop 0
	v_cvt_pk_bf16_f32 v135, v112, v113
	v_lshlrev_b32_e32 v112, 16, v187
	v_and_b32_e32 v113, 0xffff0000, v187
	v_pk_add_f32 v[112:113], v[114:115], v[112:113]
	v_cndmask_b32_e64 v114, v132, v135, s[4:5]
	v_cvt_pk_bf16_f32 v180, v112, v113
	v_cndmask_b32_e64 v112, v126, v180, s[4:5]
	v_cndmask_b32_e64 v113, v134, v133, s[4:5]
	v_cndmask_b32_e64 v115, v179, v127, s[4:5]
	ds_bpermute_b32 v181, v178, v115
	ds_bpermute_b32 v182, v178, v113
	ds_bpermute_b32 v183, v178, v114
	ds_bpermute_b32 v184, v178, v112
	v_lshl_add_u64 v[114:115], s[30:31], 0, v[208:209]
	v_lshlrev_b32_e32 v112, 1, v168
	v_mov_b32_e32 v113, v209
	v_lshl_add_u64 v[116:117], v[114:115], 0, v[112:113]
	v_lshlrev_b32_e32 v114, 1, v164
	v_mov_b32_e32 v115, v209
	v_lshl_add_u64 v[124:125], v[116:117], 0, v[114:115]
	s_waitcnt lgkmcnt(0)
	v_cndmask_b32_e64 v119, v184, v126, s[4:5]
	v_cndmask_b32_e64 v117, v182, v134, s[4:5]
	v_cndmask_b32_e64 v118, v183, v132, s[4:5]
	v_cndmask_b32_e64 v116, v181, v179, s[4:5]
	global_store_dwordx4 v[124:125], v[116:119], off nt
	v_add_co_u32_e32 v124, vcc, s25, v124
	s_nop 0
	v_cndmask_b32_e64 v119, v180, v184, s[4:5]
	v_cndmask_b32_e64 v117, v133, v182, s[4:5]
	v_cndmask_b32_e64 v118, v135, v183, s[4:5]
	v_cndmask_b32_e64 v116, v127, v181, s[4:5]
	v_addc_co_u32_e32 v125, vcc, 0, v125, vcc
	global_store_dwordx4 v[124:125], v[116:119], off nt
	s_nop 1
	v_and_b32_e32 v117, 0xffff0000, v179
	v_lshlrev_b32_e32 v116, 16, v179
	v_mul_f32_e32 v117, v117, v117
	v_and_b32_e32 v118, 0xffff0000, v134
	v_fmac_f32_e32 v117, v116, v116
	v_lshlrev_b32_e32 v116, 16, v134
	v_mul_f32_e32 v118, v118, v118
	v_fmac_f32_e32 v118, v116, v116
	v_add_f32_e32 v116, v117, v118
	v_and_b32_e32 v118, 0xffff0000, v132
	v_lshlrev_b32_e32 v117, 16, v132
	v_mul_f32_e32 v118, v118, v118
	v_fmac_f32_e32 v118, v117, v117
	v_add_f32_e32 v116, v118, v116
	v_and_b32_e32 v118, 0xffff0000, v126
	v_lshlrev_b32_e32 v117, 16, v126
	v_mul_f32_e32 v118, v118, v118
	v_fmac_f32_e32 v118, v117, v117
	v_add_f32_e32 v116, v118, v116
	v_and_b32_e32 v118, 0xffff0000, v127
	v_lshlrev_b32_e32 v117, 16, v127
	v_mul_f32_e32 v118, v118, v118
	v_and_b32_e32 v119, 0xffff0000, v133
	v_fmac_f32_e32 v118, v117, v117
	v_lshlrev_b32_e32 v117, 16, v133
	v_mul_f32_e32 v119, v119, v119
	v_fmac_f32_e32 v119, v117, v117
	v_add_f32_e32 v117, v118, v119
	v_and_b32_e32 v119, 0xffff0000, v135
	v_lshlrev_b32_e32 v118, 16, v135
	v_mul_f32_e32 v119, v119, v119
	v_fmac_f32_e32 v119, v118, v118
	v_add_f32_e32 v117, v119, v117
	v_and_b32_e32 v119, 0xffff0000, v180
	v_lshlrev_b32_e32 v118, 16, v180
	v_mul_f32_e32 v119, v119, v119
	v_fmac_f32_e32 v119, v118, v118
	v_add_f32_e32 v117, v119, v117
	v_add_f32_e32 v116, v116, v117
	ds_bpermute_b32 v117, v176, v116
	s_waitcnt lgkmcnt(0)
	v_add_f32_e32 v116, v116, v117
	ds_bpermute_b32 v117, v177, v116
	s_and_saveexec_b64 s[30:31], s[6:7]
	v_readlane_b32 s92, v253, 40
	v_readlane_b32 s93, v253, 41
	s_cbranch_execz .LBB0_1096
	s_waitcnt lgkmcnt(0)
	v_add_f32_e32 v118, v116, v117
	v_lshlrev_b64 v[116:117], 6, v[172:173]
	v_lshl_add_u64 v[116:117], s[20:21], 0, v[116:117]
	v_lshl_add_u64 v[116:117], s[10:11], 2, v[116:117]
	s_lshl_b32 s68, s55, 2
	v_lshl_add_u64 v[116:117], v[116:117], 0, s[68:69]
	global_store_dword v[116:117], v118, off

.LBB0_1102:
	s_or_b64 exec, exec, s[34:35]
	v_add_u32_e32 v64, 0x80, v172
	s_waitcnt lgkmcnt(0)
	v_ashrrev_i32_e32 v65, 31, v64
	v_lshlrev_b64 v[64:65], 11, v[64:65]
	v_lshl_add_u64 v[64:65], v[174:175], 0, v[64:65]
	v_add_u32_e32 v64, 0x90, v172
	v_ashrrev_i32_e32 v65, 31, v64
	v_lshlrev_b64 v[64:65], 11, v[64:65]
	v_lshl_add_u64 v[64:65], v[174:175], 0, v[64:65]
	v_add_u32_e32 v64, 0xa0, v172
	v_ashrrev_i32_e32 v65, 31, v64
	v_lshlrev_b64 v[64:65], 11, v[64:65]
	v_lshl_add_u64 v[64:65], v[174:175], 0, v[64:65]
	v_add_u32_e32 v64, 0xb0, v172
	v_ashrrev_i32_e32 v65, 31, v64
	v_lshlrev_b64 v[64:65], 11, v[64:65]
	v_lshl_add_u64 v[64:65], v[174:175], 0, v[64:65]
	s_nop 0
	s_waitcnt vmcnt(12)
	v_mov_b64_e32 v[88:89], v[192:193]
	v_mov_b64_e32 v[90:91], v[194:195]
	v_mov_b64_e32 v[92:93], v[196:197]
	v_mov_b64_e32 v[94:95], v[198:199]
	v_mov_b64_e32 v[84:85], v[200:201]
	v_mov_b64_e32 v[86:87], v[202:203]
	v_mov_b64_e32 v[80:81], v[204:205]
	v_mov_b64_e32 v[82:83], v[206:207]
	v_mov_b64_e32 v[76:77], v[232:233]
	v_mov_b64_e32 v[78:79], v[234:235]
	v_mov_b64_e32 v[72:73], v[236:237]
	v_mov_b64_e32 v[74:75], v[238:239]
	v_mov_b64_e32 v[68:69], v[240:241]
	v_mov_b64_e32 v[70:71], v[242:243]
	v_mov_b64_e32 v[64:65], v[244:245]
	v_mov_b64_e32 v[66:67], v[246:247]
	s_add_i32 s30, s26, 0x80
	s_ashr_i32 s31, s30, 31
	s_lshl_b64 s[34:35], s[30:31], 11
	s_add_u32 s25, s18, s34
	s_addc_u32 s27, s19, s35
	s_add_u32 s34, s25, s28
	s_addc_u32 s35, s27, s29
	v_mov_b32_e32 v113, v209
	v_mov_b32_e32 v115, v209
	s_movk_i32 s25, 0x4000
	v_lshlrev_b32_e32 v96, 16, v88
	v_and_b32_e32 v97, 0xffff0000, v88
	v_pk_add_f32 v[52:53], v[52:53], v[96:97]
	s_nop 0
	v_cvt_pk_bf16_f32 v88, v52, v53
	v_lshlrev_b32_e32 v52, 16, v89
	v_and_b32_e32 v53, 0xffff0000, v89
	v_pk_add_f32 v[52:53], v[54:55], v[52:53]
	s_nop 0
	v_cvt_pk_bf16_f32 v54, v52, v53
	v_lshlrev_b32_e32 v52, 16, v90
	v_and_b32_e32 v53, 0xffff0000, v90
	v_pk_add_f32 v[48:49], v[48:49], v[52:53]
	s_nop 0
	v_cvt_pk_bf16_f32 v53, v48, v49
	v_lshlrev_b32_e32 v48, 16, v91
	v_and_b32_e32 v49, 0xffff0000, v91
	v_pk_add_f32 v[48:49], v[50:51], v[48:49]
	s_nop 0
	v_cvt_pk_bf16_f32 v52, v48, v49
	v_lshlrev_b32_e32 v48, 16, v92
	v_and_b32_e32 v49, 0xffff0000, v92
	v_pk_add_f32 v[48:49], v[60:61], v[48:49]
	s_nop 0
	v_cvt_pk_bf16_f32 v51, v48, v49
	v_lshlrev_b32_e32 v48, 16, v93
	v_and_b32_e32 v49, 0xffff0000, v93
	v_pk_add_f32 v[48:49], v[62:63], v[48:49]
	s_nop 0
	v_cvt_pk_bf16_f32 v50, v48, v49
	v_lshlrev_b32_e32 v48, 16, v94
	v_and_b32_e32 v49, 0xffff0000, v94
	v_pk_add_f32 v[48:49], v[56:57], v[48:49]
	v_lshlrev_b32_e32 v56, 16, v95
	v_and_b32_e32 v57, 0xffff0000, v95
	v_pk_add_f32 v[56:57], v[58:59], v[56:57]
	v_cvt_pk_bf16_f32 v49, v48, v49
	v_cvt_pk_bf16_f32 v48, v56, v57
	v_cndmask_b32_e64 v55, v52, v48, s[4:5]
	v_cndmask_b32_e64 v56, v54, v50, s[4:5]
	v_cndmask_b32_e64 v57, v53, v49, s[4:5]
	v_cndmask_b32_e64 v58, v88, v51, s[4:5]
	ds_bpermute_b32 v62, v178, v58
	ds_bpermute_b32 v63, v178, v56
	ds_bpermute_b32 v89, v178, v57
	ds_bpermute_b32 v55, v178, v55
	v_lshl_add_u64 v[56:57], s[34:35], 0, v[208:209]
	v_lshl_add_u64 v[56:57], v[56:57], 0, v[112:113]
	v_lshl_add_u64 v[60:61], v[56:57], 0, v[114:115]
	s_waitcnt lgkmcnt(2)
	v_cndmask_b32_e64 v57, v63, v54, s[4:5]
	s_waitcnt lgkmcnt(0)
	v_cndmask_b32_e64 v59, v55, v52, s[4:5]
	v_cndmask_b32_e64 v58, v89, v53, s[4:5]
	v_cndmask_b32_e64 v56, v62, v88, s[4:5]
	global_store_dwordx4 v[60:61], v[56:59], off nt
	v_add_co_u32_e32 v60, vcc, s25, v60
	s_nop 0
	v_cndmask_b32_e64 v59, v48, v55, s[4:5]
	v_cndmask_b32_e64 v57, v50, v63, s[4:5]
	v_cndmask_b32_e64 v58, v49, v89, s[4:5]
	v_cndmask_b32_e64 v56, v51, v62, s[4:5]
	v_addc_co_u32_e32 v61, vcc, 0, v61, vcc
	global_store_dwordx4 v[60:61], v[56:59], off nt
	v_lshlrev_b32_e32 v55, 16, v88
	s_nop 0
	v_and_b32_e32 v56, 0xffff0000, v88
	v_mul_f32_e32 v56, v56, v56
	v_fmac_f32_e32 v56, v55, v55
	v_lshlrev_b32_e32 v55, 16, v54
	v_and_b32_e32 v54, 0xffff0000, v54
	v_mul_f32_e32 v54, v54, v54
	v_fmac_f32_e32 v54, v55, v55
	v_lshlrev_b32_e32 v55, 16, v53
	v_and_b32_e32 v53, 0xffff0000, v53
	v_mul_f32_e32 v53, v53, v53
	v_add_f32_e32 v54, v56, v54
	v_fmac_f32_e32 v53, v55, v55
	v_add_f32_e32 v53, v53, v54
	v_lshlrev_b32_e32 v54, 16, v52
	v_and_b32_e32 v52, 0xffff0000, v52
	v_mul_f32_e32 v52, v52, v52
	v_fmac_f32_e32 v52, v54, v54
	v_add_f32_e32 v52, v52, v53
	v_lshlrev_b32_e32 v53, 16, v51
	v_and_b32_e32 v51, 0xffff0000, v51
	v_mul_f32_e32 v51, v51, v51
	v_fmac_f32_e32 v51, v53, v53
	v_lshlrev_b32_e32 v53, 16, v50
	v_and_b32_e32 v50, 0xffff0000, v50
	v_mul_f32_e32 v50, v50, v50
	v_fmac_f32_e32 v50, v53, v53
	v_add_f32_e32 v50, v51, v50
	v_lshlrev_b32_e32 v51, 16, v49
	v_and_b32_e32 v49, 0xffff0000, v49
	v_mul_f32_e32 v49, v49, v49
	v_fmac_f32_e32 v49, v51, v51
	v_add_f32_e32 v49, v49, v50
	v_lshlrev_b32_e32 v50, 16, v48
	v_and_b32_e32 v48, 0xffff0000, v48
	v_mul_f32_e32 v48, v48, v48
	v_fmac_f32_e32 v48, v50, v50
	v_add_f32_e32 v48, v48, v49
	v_add_f32_e32 v48, v52, v48
	ds_bpermute_b32 v49, v176, v48
	s_waitcnt lgkmcnt(0)
	v_add_f32_e32 v48, v48, v49
	ds_bpermute_b32 v49, v177, v48
	s_and_saveexec_b64 s[34:35], s[6:7]
	s_cbranch_execz .LBB0_1104
	s_waitcnt lgkmcnt(0)
	v_add_f32_e32 v50, v48, v49
	v_or_b32_e32 v48, s30, v165
	v_ashrrev_i32_e32 v49, 31, v48
	v_lshlrev_b64 v[48:49], 6, v[48:49]
	v_lshl_add_u64 v[48:49], s[20:21], 0, v[48:49]
	v_lshl_add_u64 v[48:49], s[10:11], 2, v[48:49]
	s_lshl_b32 s68, s55, 2
	v_lshl_add_u64 v[48:49], v[48:49], 0, s[68:69]
	global_store_dword v[48:49], v50, off
.LBB0_1104:
	s_or_b64 exec, exec, s[34:35]
	v_lshlrev_b32_e32 v48, 16, v84
	s_waitcnt lgkmcnt(0)
	v_and_b32_e32 v49, 0xffff0000, v84
	v_pk_add_f32 v[36:37], v[36:37], v[48:49]
	s_add_i32 s30, s26, 0x90
	v_cvt_pk_bf16_f32 v48, v36, v37
	v_lshlrev_b32_e32 v36, 16, v85
	v_and_b32_e32 v37, 0xffff0000, v85
	v_pk_add_f32 v[36:37], v[38:39], v[36:37]
	s_ashr_i32 s31, s30, 31
	v_cvt_pk_bf16_f32 v49, v36, v37
	v_lshlrev_b32_e32 v36, 16, v86
	v_and_b32_e32 v37, 0xffff0000, v86
	v_pk_add_f32 v[32:33], v[32:33], v[36:37]
	s_lshl_b64 s[34:35], s[30:31], 11
	v_cvt_pk_bf16_f32 v36, v32, v33
	v_lshlrev_b32_e32 v32, 16, v87
	v_and_b32_e32 v33, 0xffff0000, v87
	v_pk_add_f32 v[32:33], v[34:35], v[32:33]
	s_add_u32 s25, s18, s34
	v_cvt_pk_bf16_f32 v37, v32, v33
	v_lshlrev_b32_e32 v32, 16, v80
	v_and_b32_e32 v33, 0xffff0000, v80
	v_pk_add_f32 v[32:33], v[44:45], v[32:33]
	s_addc_u32 s27, s19, s35
	v_cvt_pk_bf16_f32 v44, v32, v33
	v_lshlrev_b32_e32 v32, 16, v81
	v_and_b32_e32 v33, 0xffff0000, v81
	v_pk_add_f32 v[32:33], v[46:47], v[32:33]
	v_cndmask_b32_e64 v35, v48, v44, s[4:5]
	v_cvt_pk_bf16_f32 v45, v32, v33
	v_lshlrev_b32_e32 v32, 16, v82
	v_and_b32_e32 v33, 0xffff0000, v82
	v_pk_add_f32 v[32:33], v[40:41], v[32:33]
	s_add_u32 s34, s25, s28
	v_cvt_pk_bf16_f32 v40, v32, v33
	v_lshlrev_b32_e32 v32, 16, v83
	v_and_b32_e32 v33, 0xffff0000, v83
	v_pk_add_f32 v[32:33], v[42:43], v[32:33]
	v_cndmask_b32_e64 v34, v36, v40, s[4:5]
	v_cvt_pk_bf16_f32 v41, v32, v33
	v_cndmask_b32_e64 v32, v37, v41, s[4:5]
	v_cndmask_b32_e64 v33, v49, v45, s[4:5]
	ds_bpermute_b32 v42, v178, v35
	ds_bpermute_b32 v43, v178, v33
	ds_bpermute_b32 v46, v178, v32
	ds_bpermute_b32 v47, v178, v34
	s_addc_u32 s35, s27, s29
	v_lshl_add_u64 v[32:33], s[34:35], 0, v[208:209]
	v_lshl_add_u64 v[32:33], v[32:33], 0, v[112:113]
	v_lshl_add_u64 v[38:39], v[32:33], 0, v[114:115]
	s_waitcnt lgkmcnt(1)
	v_cndmask_b32_e64 v35, v46, v37, s[4:5]
	v_cndmask_b32_e64 v33, v43, v49, s[4:5]
	s_waitcnt lgkmcnt(0)
	v_cndmask_b32_e64 v34, v47, v36, s[4:5]
	v_cndmask_b32_e64 v32, v42, v48, s[4:5]
	global_store_dwordx4 v[38:39], v[32:35], off nt
	s_movk_i32 s25, 0x4000
	v_add_co_u32_e32 v38, vcc, s25, v38
	v_and_b32_e32 v33, 0xffff0000, v48
	v_lshlrev_b32_e32 v32, 16, v48
	v_mul_f32_e32 v33, v33, v33
	v_and_b32_e32 v34, 0xffff0000, v49
	v_fmac_f32_e32 v33, v32, v32
	v_lshlrev_b32_e32 v32, 16, v49
	v_mul_f32_e32 v34, v34, v34
	v_fmac_f32_e32 v34, v32, v32
	v_add_f32_e32 v32, v33, v34
	v_and_b32_e32 v34, 0xffff0000, v36
	v_lshlrev_b32_e32 v33, 16, v36
	v_mul_f32_e32 v34, v34, v34
	v_fmac_f32_e32 v34, v33, v33
	v_add_f32_e32 v32, v34, v32
	v_and_b32_e32 v34, 0xffff0000, v37
	v_lshlrev_b32_e32 v33, 16, v37
	v_mul_f32_e32 v34, v34, v34
	v_fmac_f32_e32 v34, v33, v33
	v_add_f32_e32 v32, v34, v32
	v_and_b32_e32 v34, 0xffff0000, v44
	v_lshlrev_b32_e32 v33, 16, v44
	v_mul_f32_e32 v34, v34, v34
	v_and_b32_e32 v35, 0xffff0000, v45
	v_fmac_f32_e32 v34, v33, v33
	v_lshlrev_b32_e32 v33, 16, v45
	v_mul_f32_e32 v35, v35, v35
	v_fmac_f32_e32 v35, v33, v33
	v_add_f32_e32 v33, v34, v35
	v_and_b32_e32 v35, 0xffff0000, v40
	v_lshlrev_b32_e32 v34, 16, v40
	v_mul_f32_e32 v35, v35, v35
	v_fmac_f32_e32 v35, v34, v34
	v_add_f32_e32 v33, v35, v33
	v_and_b32_e32 v35, 0xffff0000, v41
	v_lshlrev_b32_e32 v34, 16, v41
	v_mul_f32_e32 v35, v35, v35
	v_fmac_f32_e32 v35, v34, v34
	v_add_f32_e32 v33, v35, v33
	v_add_f32_e32 v32, v32, v33
	ds_bpermute_b32 v33, v176, v32
	v_cndmask_b32_e64 v37, v41, v46, s[4:5]
	v_cndmask_b32_e64 v35, v45, v43, s[4:5]
	v_cndmask_b32_e64 v36, v40, v47, s[4:5]
	v_cndmask_b32_e64 v34, v44, v42, s[4:5]
	s_waitcnt lgkmcnt(0)
	v_add_f32_e32 v32, v32, v33
	ds_bpermute_b32 v33, v177, v32
	v_addc_co_u32_e32 v39, vcc, 0, v39, vcc
	global_store_dwordx4 v[38:39], v[34:37], off nt
	s_and_saveexec_b64 s[34:35], s[6:7]
	s_cbranch_execz .LBB0_1106
	s_waitcnt lgkmcnt(0)
	v_add_f32_e32 v34, v32, v33
	v_or_b32_e32 v32, s30, v165
	v_ashrrev_i32_e32 v33, 31, v32
	v_lshlrev_b64 v[32:33], 6, v[32:33]
	v_lshl_add_u64 v[32:33], s[20:21], 0, v[32:33]
	v_lshl_add_u64 v[32:33], s[10:11], 2, v[32:33]
	s_lshl_b32 s68, s55, 2
	v_lshl_add_u64 v[32:33], v[32:33], 0, s[68:69]
	global_store_dword v[32:33], v34, off
.LBB0_1106:
	s_or_b64 exec, exec, s[34:35]
	v_lshlrev_b32_e32 v32, 16, v76
	s_waitcnt lgkmcnt(0)
	v_and_b32_e32 v33, 0xffff0000, v76
	v_pk_add_f32 v[20:21], v[20:21], v[32:33]
	s_add_i32 s30, s26, 0xa0
	v_cvt_pk_bf16_f32 v32, v20, v21
	v_lshlrev_b32_e32 v20, 16, v77
	v_and_b32_e32 v21, 0xffff0000, v77
	v_pk_add_f32 v[20:21], v[22:23], v[20:21]
	s_ashr_i32 s31, s30, 31
	v_cvt_pk_bf16_f32 v33, v20, v21
	v_lshlrev_b32_e32 v20, 16, v78
	v_and_b32_e32 v21, 0xffff0000, v78
	v_pk_add_f32 v[16:17], v[16:17], v[20:21]
	s_lshl_b64 s[34:35], s[30:31], 11
	v_cvt_pk_bf16_f32 v20, v16, v17
	v_lshlrev_b32_e32 v16, 16, v79
	v_and_b32_e32 v17, 0xffff0000, v79
	v_pk_add_f32 v[16:17], v[18:19], v[16:17]
	s_add_u32 s25, s18, s34
	v_cvt_pk_bf16_f32 v21, v16, v17
	v_lshlrev_b32_e32 v16, 16, v72
	v_and_b32_e32 v17, 0xffff0000, v72
	v_pk_add_f32 v[16:17], v[28:29], v[16:17]
	s_addc_u32 s27, s19, s35
	v_cvt_pk_bf16_f32 v28, v16, v17
	v_lshlrev_b32_e32 v16, 16, v73
	v_and_b32_e32 v17, 0xffff0000, v73
	v_pk_add_f32 v[16:17], v[30:31], v[16:17]
	v_cndmask_b32_e64 v19, v32, v28, s[4:5]
	v_cvt_pk_bf16_f32 v29, v16, v17
	v_lshlrev_b32_e32 v16, 16, v74
	v_and_b32_e32 v17, 0xffff0000, v74
	v_pk_add_f32 v[16:17], v[24:25], v[16:17]
	s_add_u32 s34, s25, s28
	v_cvt_pk_bf16_f32 v24, v16, v17
	v_lshlrev_b32_e32 v16, 16, v75
	v_and_b32_e32 v17, 0xffff0000, v75
	v_pk_add_f32 v[16:17], v[26:27], v[16:17]
	v_cndmask_b32_e64 v18, v20, v24, s[4:5]
	v_cvt_pk_bf16_f32 v25, v16, v17
	v_cndmask_b32_e64 v16, v21, v25, s[4:5]
	v_cndmask_b32_e64 v17, v33, v29, s[4:5]
	ds_bpermute_b32 v26, v178, v19
	ds_bpermute_b32 v27, v178, v17
	ds_bpermute_b32 v30, v178, v18
	ds_bpermute_b32 v31, v178, v16
	s_addc_u32 s35, s27, s29
	v_lshl_add_u64 v[16:17], s[34:35], 0, v[208:209]
	v_mov_b32_e32 v113, v209
	v_lshl_add_u64 v[16:17], v[16:17], 0, v[112:113]
	v_mov_b32_e32 v115, v209
	v_lshl_add_u64 v[22:23], v[16:17], 0, v[114:115]
	s_waitcnt lgkmcnt(0)
	v_cndmask_b32_e64 v19, v31, v21, s[4:5]
	v_cndmask_b32_e64 v17, v27, v33, s[4:5]
	v_cndmask_b32_e64 v18, v30, v20, s[4:5]
	v_cndmask_b32_e64 v16, v26, v32, s[4:5]
	global_store_dwordx4 v[22:23], v[16:19], off nt
	s_movk_i32 s25, 0x4000
	v_add_co_u32_e32 v22, vcc, s25, v22
	v_and_b32_e32 v17, 0xffff0000, v32
	v_lshlrev_b32_e32 v16, 16, v32
	v_mul_f32_e32 v17, v17, v17
	v_and_b32_e32 v18, 0xffff0000, v33
	v_fmac_f32_e32 v17, v16, v16
	v_lshlrev_b32_e32 v16, 16, v33
	v_mul_f32_e32 v18, v18, v18
	v_fmac_f32_e32 v18, v16, v16
	v_add_f32_e32 v16, v17, v18
	v_and_b32_e32 v18, 0xffff0000, v20
	v_lshlrev_b32_e32 v17, 16, v20
	v_mul_f32_e32 v18, v18, v18
	v_fmac_f32_e32 v18, v17, v17
	v_add_f32_e32 v16, v18, v16
	v_and_b32_e32 v18, 0xffff0000, v21
	v_lshlrev_b32_e32 v17, 16, v21
	v_mul_f32_e32 v18, v18, v18
	v_fmac_f32_e32 v18, v17, v17
	v_add_f32_e32 v16, v18, v16
	v_and_b32_e32 v18, 0xffff0000, v28
	v_lshlrev_b32_e32 v17, 16, v28
	v_mul_f32_e32 v18, v18, v18
	v_and_b32_e32 v19, 0xffff0000, v29
	v_fmac_f32_e32 v18, v17, v17
	v_lshlrev_b32_e32 v17, 16, v29
	v_mul_f32_e32 v19, v19, v19
	v_fmac_f32_e32 v19, v17, v17
	v_add_f32_e32 v17, v18, v19
	v_and_b32_e32 v19, 0xffff0000, v24
	v_lshlrev_b32_e32 v18, 16, v24
	v_mul_f32_e32 v19, v19, v19
	v_fmac_f32_e32 v19, v18, v18
	v_add_f32_e32 v17, v19, v17
	v_and_b32_e32 v19, 0xffff0000, v25
	v_lshlrev_b32_e32 v18, 16, v25
	v_mul_f32_e32 v19, v19, v19
	v_fmac_f32_e32 v19, v18, v18
	v_add_f32_e32 v17, v19, v17
	v_add_f32_e32 v16, v16, v17
	ds_bpermute_b32 v17, v176, v16
	v_cndmask_b32_e64 v21, v25, v31, s[4:5]
	v_cndmask_b32_e64 v19, v29, v27, s[4:5]
	v_cndmask_b32_e64 v20, v24, v30, s[4:5]
	v_cndmask_b32_e64 v18, v28, v26, s[4:5]
	s_waitcnt lgkmcnt(0)
	v_add_f32_e32 v16, v16, v17
	ds_bpermute_b32 v17, v177, v16
	v_addc_co_u32_e32 v23, vcc, 0, v23, vcc
	global_store_dwordx4 v[22:23], v[18:21], off nt
	s_and_saveexec_b64 s[34:35], s[6:7]
	s_cbranch_execz .LBB0_1108
	s_waitcnt lgkmcnt(0)
	v_add_f32_e32 v18, v16, v17
	v_or_b32_e32 v16, s30, v165
	v_ashrrev_i32_e32 v17, 31, v16
	v_lshlrev_b64 v[16:17], 6, v[16:17]
	v_lshl_add_u64 v[16:17], s[20:21], 0, v[16:17]
	v_lshl_add_u64 v[16:17], s[10:11], 2, v[16:17]
	s_lshl_b32 s68, s55, 2
	v_lshl_add_u64 v[16:17], v[16:17], 0, s[68:69]
	global_store_dword v[16:17], v18, off
.LBB0_1108:
	s_or_b64 exec, exec, s[34:35]
	v_lshlrev_b32_e32 v16, 16, v68
	s_waitcnt lgkmcnt(0)
	v_and_b32_e32 v17, 0xffff0000, v68
	v_pk_add_f32 v[4:5], v[4:5], v[16:17]
	s_addk_i32 s26, 0xb0
	v_cvt_pk_bf16_f32 v16, v4, v5
	v_lshlrev_b32_e32 v4, 16, v69
	v_and_b32_e32 v5, 0xffff0000, v69
	v_pk_add_f32 v[4:5], v[6:7], v[4:5]
	s_ashr_i32 s27, s26, 31
	v_cvt_pk_bf16_f32 v17, v4, v5
	v_lshlrev_b32_e32 v4, 16, v70
	v_and_b32_e32 v5, 0xffff0000, v70
	v_pk_add_f32 v[0:1], v[0:1], v[4:5]
	s_lshl_b64 s[30:31], s[26:27], 11
	v_cvt_pk_bf16_f32 v4, v0, v1
	v_lshlrev_b32_e32 v0, 16, v71
	v_and_b32_e32 v1, 0xffff0000, v71
	v_pk_add_f32 v[0:1], v[2:3], v[0:1]
	s_add_u32 s25, s18, s30
	v_cvt_pk_bf16_f32 v5, v0, v1
	v_lshlrev_b32_e32 v0, 16, v64
	v_and_b32_e32 v1, 0xffff0000, v64
	v_pk_add_f32 v[0:1], v[12:13], v[0:1]
	s_addc_u32 s27, s19, s31
	v_cvt_pk_bf16_f32 v12, v0, v1
	v_lshlrev_b32_e32 v0, 16, v65
	v_and_b32_e32 v1, 0xffff0000, v65
	v_pk_add_f32 v[0:1], v[14:15], v[0:1]
	v_cndmask_b32_e64 v3, v16, v12, s[4:5]
	v_cvt_pk_bf16_f32 v13, v0, v1
	v_lshlrev_b32_e32 v0, 16, v66
	v_and_b32_e32 v1, 0xffff0000, v66
	v_pk_add_f32 v[0:1], v[8:9], v[0:1]
	s_add_u32 s28, s25, s28
	v_cvt_pk_bf16_f32 v8, v0, v1
	v_lshlrev_b32_e32 v0, 16, v67
	v_and_b32_e32 v1, 0xffff0000, v67
	v_pk_add_f32 v[0:1], v[10:11], v[0:1]
	v_cndmask_b32_e64 v2, v4, v8, s[4:5]
	v_cvt_pk_bf16_f32 v9, v0, v1
	v_cndmask_b32_e64 v0, v5, v9, s[4:5]
	v_cndmask_b32_e64 v1, v17, v13, s[4:5]
	ds_bpermute_b32 v10, v178, v3
	ds_bpermute_b32 v11, v178, v1
	ds_bpermute_b32 v14, v178, v0
	ds_bpermute_b32 v15, v178, v2
	s_addc_u32 s29, s27, s29
	v_lshl_add_u64 v[0:1], s[28:29], 0, v[208:209]
	v_lshl_add_u64 v[0:1], v[0:1], 0, v[112:113]
	v_lshl_add_u64 v[6:7], v[0:1], 0, v[114:115]
	s_waitcnt lgkmcnt(1)
	v_cndmask_b32_e64 v3, v14, v5, s[4:5]
	v_cndmask_b32_e64 v1, v11, v17, s[4:5]
	s_waitcnt lgkmcnt(0)
	v_cndmask_b32_e64 v2, v15, v4, s[4:5]
	v_cndmask_b32_e64 v0, v10, v16, s[4:5]
	global_store_dwordx4 v[6:7], v[0:3], off nt
	s_movk_i32 s25, 0x4000
	v_add_co_u32_e32 v6, vcc, s25, v6
	v_and_b32_e32 v1, 0xffff0000, v16
	v_lshlrev_b32_e32 v0, 16, v16
	v_mul_f32_e32 v1, v1, v1
	v_and_b32_e32 v2, 0xffff0000, v17
	v_fmac_f32_e32 v1, v0, v0
	v_lshlrev_b32_e32 v0, 16, v17
	v_mul_f32_e32 v2, v2, v2
	v_fmac_f32_e32 v2, v0, v0
	v_add_f32_e32 v0, v1, v2
	v_and_b32_e32 v2, 0xffff0000, v4
	v_lshlrev_b32_e32 v1, 16, v4
	v_mul_f32_e32 v2, v2, v2
	v_fmac_f32_e32 v2, v1, v1
	v_add_f32_e32 v0, v2, v0
	v_and_b32_e32 v2, 0xffff0000, v5
	v_lshlrev_b32_e32 v1, 16, v5
	v_mul_f32_e32 v2, v2, v2
	v_fmac_f32_e32 v2, v1, v1
	v_add_f32_e32 v0, v2, v0
	v_and_b32_e32 v2, 0xffff0000, v12
	v_lshlrev_b32_e32 v1, 16, v12
	v_mul_f32_e32 v2, v2, v2
	v_and_b32_e32 v3, 0xffff0000, v13
	v_fmac_f32_e32 v2, v1, v1
	v_lshlrev_b32_e32 v1, 16, v13
	v_mul_f32_e32 v3, v3, v3
	v_fmac_f32_e32 v3, v1, v1
	v_add_f32_e32 v1, v2, v3
	v_and_b32_e32 v3, 0xffff0000, v8
	v_lshlrev_b32_e32 v2, 16, v8
	v_mul_f32_e32 v3, v3, v3
	v_fmac_f32_e32 v3, v2, v2
	v_add_f32_e32 v1, v3, v1
	v_and_b32_e32 v3, 0xffff0000, v9
	v_lshlrev_b32_e32 v2, 16, v9
	v_mul_f32_e32 v3, v3, v3
	v_fmac_f32_e32 v3, v2, v2
	v_add_f32_e32 v1, v3, v1
	v_add_f32_e32 v0, v0, v1
	ds_bpermute_b32 v1, v176, v0
	v_cndmask_b32_e64 v5, v9, v14, s[4:5]
	v_cndmask_b32_e64 v3, v13, v11, s[4:5]
	v_cndmask_b32_e64 v4, v8, v15, s[4:5]
	v_cndmask_b32_e64 v2, v12, v10, s[4:5]
	s_waitcnt lgkmcnt(0)
	v_add_f32_e32 v0, v0, v1
	ds_bpermute_b32 v1, v177, v0
	v_addc_co_u32_e32 v7, vcc, 0, v7, vcc
	global_store_dwordx4 v[6:7], v[2:5], off nt
	s_and_saveexec_b64 s[28:29], s[6:7]
	s_cbranch_execz .LBB0_1110
	s_waitcnt lgkmcnt(0)
	v_add_f32_e32 v2, v0, v1
	v_or_b32_e32 v0, s26, v165
	v_ashrrev_i32_e32 v1, 31, v0
	v_lshlrev_b64 v[0:1], 6, v[0:1]
	v_lshl_add_u64 v[0:1], s[20:21], 0, v[0:1]
	v_lshl_add_u64 v[0:1], s[10:11], 2, v[0:1]
	s_lshl_b32 s68, s55, 2
	v_lshl_add_u64 v[0:1], v[0:1], 0, s[68:69]
	global_store_dword v[0:1], v2, off

.LBB0_1339:
	s_lshl_b32 s23, s28, 8
	s_add_i32 s28, s23, s59
	s_lshl_b32 s23, s26, 8
	s_or_b32 s30, s23, s70
	v_or_b32_e32 v172, s28, v165
	s_ashr_i32 s31, s30, 31
	s_lshl_b64 s[30:31], s[30:31], 1
	v_ashrrev_i32_e32 v173, 31, v172
	v_lshl_add_u64 v[174:175], v[170:171], 0, s[30:31]
	v_lshlrev_b64 v[128:129], 11, v[172:173]
	v_lshl_add_u64 v[128:129], v[174:175], 0, v[128:129]
	global_load_dwordx4 v[180:183], v[128:129], off
	global_load_dwordx4 v[184:187], v[128:129], off offset:64
	v_or_b32_e32 v128, 16, v172
	v_ashrrev_i32_e32 v129, 31, v128
	v_lshlrev_b64 v[128:129], 11, v[128:129]
	v_lshl_add_u64 v[128:129], v[174:175], 0, v[128:129]
	global_load_dwordx4 v[148:151], v[128:129], off
	global_load_dwordx4 v[144:147], v[128:129], off offset:64
	v_or_b32_e32 v128, 32, v172
	v_ashrrev_i32_e32 v129, 31, v128
	v_lshlrev_b64 v[128:129], 11, v[128:129]
	v_lshl_add_u64 v[128:129], v[174:175], 0, v[128:129]
	global_load_dwordx4 v[140:143], v[128:129], off
	global_load_dwordx4 v[136:139], v[128:129], off offset:64
	v_or_b32_e32 v128, 48, v172
	v_ashrrev_i32_e32 v129, 31, v128
	v_lshlrev_b64 v[128:129], 11, v[128:129]
	v_lshl_add_u64 v[128:129], v[174:175], 0, v[128:129]
	global_load_dwordx4 v[132:135], v[128:129], off
	s_nop 0
	global_load_dwordx4 v[128:131], v[128:129], off offset:64
	v_add_u32_e32 v214, 0x80, v172
	v_ashrrev_i32_e32 v215, 31, v214
	v_lshlrev_b64 v[214:215], 11, v[214:215]
	v_lshl_add_u64 v[214:215], v[174:175], 0, v[214:215]
	global_load_dwordx4 v[192:195], v[214:215], off
	global_load_dwordx4 v[196:199], v[214:215], off offset:64
	v_add_u32_e32 v214, 0x90, v172
	v_ashrrev_i32_e32 v215, 31, v214
	v_lshlrev_b64 v[214:215], 11, v[214:215]
	v_lshl_add_u64 v[214:215], v[174:175], 0, v[214:215]
	global_load_dwordx4 v[200:203], v[214:215], off
	global_load_dwordx4 v[204:207], v[214:215], off offset:64
	v_add_u32_e32 v214, 0xa0, v172
	v_ashrrev_i32_e32 v215, 31, v214
	v_lshlrev_b64 v[214:215], 11, v[214:215]
	v_lshl_add_u64 v[214:215], v[174:175], 0, v[214:215]
	global_load_dwordx4 v[232:235], v[214:215], off
	global_load_dwordx4 v[236:239], v[214:215], off offset:64
	v_add_u32_e32 v214, 0xb0, v172
	v_ashrrev_i32_e32 v215, 31, v214
	v_lshlrev_b64 v[214:215], 11, v[214:215]
	v_lshl_add_u64 v[214:215], v[174:175], 0, v[214:215]
	global_load_dwordx4 v[240:243], v[214:215], off
	global_load_dwordx4 v[244:247], v[214:215], off offset:64
	v_and_b32_e32 v177, 64, v225
	v_xor_b32_e32 v176, 8, v225
	v_add_u32_e32 v177, 64, v177
	v_cmp_lt_i32_e32 vcc, v176, v177
	v_xor_b32_e32 v179, 32, v225
	s_lshl_b32 s26, s26, 2
	v_cndmask_b32_e32 v176, v225, v176, vcc
	v_lshlrev_b32_e32 v178, 2, v176
	v_xor_b32_e32 v176, 16, v225
	v_cmp_lt_i32_e32 vcc, v176, v177
	s_ashr_i32 s29, s28, 31
	s_ashr_i32 s27, s26, 31
	v_cndmask_b32_e32 v176, v225, v176, vcc
	v_cmp_lt_i32_e32 vcc, v179, v177
	s_lshl_b64 s[34:35], s[28:29], 11
	s_add_u32 s23, s14, s34
	v_cndmask_b32_e32 v177, v225, v179, vcc
	s_addc_u32 s25, s15, s35
	s_add_u32 s34, s23, s30
	s_addc_u32 s35, s25, s31
	v_lshlrev_b32_e32 v208, 1, v166
	s_movk_i32 s23, 0x4000
	v_lshlrev_b32_e32 v176, 2, v176
	v_lshlrev_b32_e32 v177, 2, v177
	s_waitcnt vmcnt(8)
	v_lshlrev_b32_e32 v188, 16, v180
	v_and_b32_e32 v189, 0xffff0000, v180
	v_pk_add_f32 v[124:125], v[124:125], v[188:189]
	s_nop 0
	v_cvt_pk_bf16_f32 v179, v124, v125
	v_lshlrev_b32_e32 v124, 16, v181
	v_and_b32_e32 v125, 0xffff0000, v181
	v_pk_add_f32 v[124:125], v[126:127], v[124:125]
	s_nop 0
	v_cvt_pk_bf16_f32 v126, v124, v125
	v_lshlrev_b32_e32 v124, 16, v182
	v_and_b32_e32 v125, 0xffff0000, v182
	v_pk_add_f32 v[120:121], v[120:121], v[124:125]
	s_nop 0
	v_cvt_pk_bf16_f32 v124, v120, v121
	v_lshlrev_b32_e32 v120, 16, v183
	v_and_b32_e32 v121, 0xffff0000, v183
	v_pk_add_f32 v[120:121], v[122:123], v[120:121]
	s_nop 0
	v_cvt_pk_bf16_f32 v125, v120, v121
	v_lshlrev_b32_e32 v120, 16, v184
	v_and_b32_e32 v121, 0xffff0000, v184
	v_pk_add_f32 v[116:117], v[116:117], v[120:121]
	s_nop 0
	v_cvt_pk_bf16_f32 v127, v116, v117
	v_lshlrev_b32_e32 v116, 16, v185
	v_and_b32_e32 v117, 0xffff0000, v185
	v_pk_add_f32 v[116:117], v[118:119], v[116:117]
	s_nop 0
	v_cvt_pk_bf16_f32 v180, v116, v117
	v_lshlrev_b32_e32 v116, 16, v186
	v_and_b32_e32 v117, 0xffff0000, v186
	v_pk_add_f32 v[112:113], v[112:113], v[116:117]
	s_nop 0
	v_cvt_pk_bf16_f32 v117, v112, v113
	v_lshlrev_b32_e32 v112, 16, v187
	v_and_b32_e32 v113, 0xffff0000, v187
	v_pk_add_f32 v[112:113], v[114:115], v[112:113]
	v_cndmask_b32_e64 v114, v124, v117, s[4:5]
	v_cvt_pk_bf16_f32 v116, v112, v113
	v_cndmask_b32_e64 v112, v125, v116, s[4:5]
	v_cndmask_b32_e64 v113, v126, v180, s[4:5]
	v_cndmask_b32_e64 v115, v179, v127, s[4:5]
	ds_bpermute_b32 v181, v178, v115
	ds_bpermute_b32 v182, v178, v113
	ds_bpermute_b32 v183, v178, v114
	ds_bpermute_b32 v184, v178, v112
	v_lshl_add_u64 v[114:115], s[34:35], 0, v[208:209]
	v_lshlrev_b32_e32 v112, 1, v168
	v_mov_b32_e32 v113, v209
	v_lshl_add_u64 v[118:119], v[114:115], 0, v[112:113]
	v_lshlrev_b32_e32 v114, 1, v164
	v_mov_b32_e32 v115, v209
	v_lshl_add_u64 v[122:123], v[118:119], 0, v[114:115]
	s_waitcnt lgkmcnt(0)
	v_cndmask_b32_e64 v121, v184, v125, s[4:5]
	v_cndmask_b32_e64 v119, v182, v126, s[4:5]
	v_cndmask_b32_e64 v120, v183, v124, s[4:5]
	v_cndmask_b32_e64 v118, v181, v179, s[4:5]
	global_store_dwordx4 v[122:123], v[118:121], off nt
	v_add_co_u32_e32 v122, vcc, s23, v122
	s_nop 0
	v_cndmask_b32_e64 v121, v116, v184, s[4:5]
	v_cndmask_b32_e64 v119, v180, v182, s[4:5]
	v_cndmask_b32_e64 v120, v117, v183, s[4:5]
	v_cndmask_b32_e64 v118, v127, v181, s[4:5]
	v_addc_co_u32_e32 v123, vcc, 0, v123, vcc
	global_store_dwordx4 v[122:123], v[118:121], off nt
	s_nop 1
	v_and_b32_e32 v119, 0xffff0000, v179
	v_lshlrev_b32_e32 v118, 16, v179
	v_mul_f32_e32 v119, v119, v119
	v_and_b32_e32 v120, 0xffff0000, v126
	v_fmac_f32_e32 v119, v118, v118
	v_lshlrev_b32_e32 v118, 16, v126
	v_mul_f32_e32 v120, v120, v120
	v_fmac_f32_e32 v120, v118, v118
	v_add_f32_e32 v118, v119, v120
	v_and_b32_e32 v120, 0xffff0000, v124
	v_lshlrev_b32_e32 v119, 16, v124
	v_mul_f32_e32 v120, v120, v120
	v_fmac_f32_e32 v120, v119, v119
	v_add_f32_e32 v118, v120, v118
	v_and_b32_e32 v120, 0xffff0000, v125
	v_lshlrev_b32_e32 v119, 16, v125
	v_mul_f32_e32 v120, v120, v120
	v_fmac_f32_e32 v120, v119, v119
	v_add_f32_e32 v118, v120, v118
	v_and_b32_e32 v120, 0xffff0000, v127
	v_lshlrev_b32_e32 v119, 16, v127
	v_mul_f32_e32 v120, v120, v120
	v_and_b32_e32 v121, 0xffff0000, v180
	v_fmac_f32_e32 v120, v119, v119
	v_lshlrev_b32_e32 v119, 16, v180
	v_mul_f32_e32 v121, v121, v121
	v_fmac_f32_e32 v121, v119, v119
	v_add_f32_e32 v119, v120, v121
	v_lshlrev_b32_e32 v120, 16, v117
	v_and_b32_e32 v117, 0xffff0000, v117
	v_mul_f32_e32 v117, v117, v117
	v_fmac_f32_e32 v117, v120, v120
	v_add_f32_e32 v117, v117, v119
	v_lshlrev_b32_e32 v119, 16, v116
	v_and_b32_e32 v116, 0xffff0000, v116
	v_mul_f32_e32 v116, v116, v116
	v_fmac_f32_e32 v116, v119, v119
	v_add_f32_e32 v116, v116, v117
	v_add_f32_e32 v116, v118, v116
	ds_bpermute_b32 v117, v176, v116
	s_waitcnt lgkmcnt(0)
	v_add_f32_e32 v116, v116, v117
	ds_bpermute_b32 v117, v177, v116
	s_and_saveexec_b64 s[34:35], s[6:7]
	s_cbranch_execz .LBB0_1341
	s_waitcnt lgkmcnt(0)
	v_add_f32_e32 v118, v116, v117
	v_lshlrev_b64 v[116:117], 6, v[172:173]
	v_lshl_add_u64 v[116:117], s[16:17], 0, v[116:117]
	v_lshl_add_u64 v[116:117], s[26:27], 2, v[116:117]
	s_lshl_b32 s68, s58, 2
	v_lshl_add_u64 v[116:117], v[116:117], 0, s[68:69]
	global_store_dword v[116:117], v118, off

.LBB0_1347:
	s_or_b64 exec, exec, s[36:37]
	v_add_u32_e32 v64, 0x80, v172
	s_waitcnt lgkmcnt(0)
	v_ashrrev_i32_e32 v65, 31, v64
	v_lshlrev_b64 v[64:65], 11, v[64:65]
	v_lshl_add_u64 v[64:65], v[174:175], 0, v[64:65]
	v_add_u32_e32 v64, 0x90, v172
	v_ashrrev_i32_e32 v65, 31, v64
	v_lshlrev_b64 v[64:65], 11, v[64:65]
	v_lshl_add_u64 v[64:65], v[174:175], 0, v[64:65]
	v_add_u32_e32 v64, 0xa0, v172
	v_ashrrev_i32_e32 v65, 31, v64
	v_lshlrev_b64 v[64:65], 11, v[64:65]
	v_lshl_add_u64 v[64:65], v[174:175], 0, v[64:65]
	v_add_u32_e32 v64, 0xb0, v172
	v_ashrrev_i32_e32 v65, 31, v64
	v_lshlrev_b64 v[64:65], 11, v[64:65]
	v_lshl_add_u64 v[64:65], v[174:175], 0, v[64:65]
	s_nop 0
	s_waitcnt vmcnt(12)
	v_mov_b64_e32 v[88:89], v[192:193]
	v_mov_b64_e32 v[90:91], v[194:195]
	v_mov_b64_e32 v[92:93], v[196:197]
	v_mov_b64_e32 v[94:95], v[198:199]
	v_mov_b64_e32 v[84:85], v[200:201]
	v_mov_b64_e32 v[86:87], v[202:203]
	v_mov_b64_e32 v[80:81], v[204:205]
	v_mov_b64_e32 v[82:83], v[206:207]
	v_mov_b64_e32 v[76:77], v[232:233]
	v_mov_b64_e32 v[78:79], v[234:235]
	v_mov_b64_e32 v[72:73], v[236:237]
	v_mov_b64_e32 v[74:75], v[238:239]
	v_mov_b64_e32 v[68:69], v[240:241]
	v_mov_b64_e32 v[70:71], v[242:243]
	v_mov_b64_e32 v[64:65], v[244:245]
	v_mov_b64_e32 v[66:67], v[246:247]
	s_add_i32 s34, s28, 0x80
	s_ashr_i32 s35, s34, 31
	s_lshl_b64 s[36:37], s[34:35], 11
	s_add_u32 s23, s14, s36
	s_addc_u32 s25, s15, s37
	s_add_u32 s36, s23, s30
	s_addc_u32 s37, s25, s31
	v_mov_b32_e32 v113, v209
	v_mov_b32_e32 v115, v209
	s_movk_i32 s23, 0x4000
	v_lshlrev_b32_e32 v96, 16, v88
	v_and_b32_e32 v97, 0xffff0000, v88
	v_lshlrev_b32_e32 v88, 16, v89
	v_and_b32_e32 v89, 0xffff0000, v89
	v_pk_add_f32 v[60:61], v[60:61], v[96:97]
	v_pk_add_f32 v[62:63], v[62:63], v[88:89]
	v_cvt_pk_bf16_f32 v61, v60, v61
	v_cvt_pk_bf16_f32 v60, v62, v63
	v_lshlrev_b32_e32 v62, 16, v90
	v_and_b32_e32 v63, 0xffff0000, v90
	v_pk_add_f32 v[56:57], v[56:57], v[62:63]
	v_lshlrev_b32_e32 v62, 16, v91
	v_and_b32_e32 v63, 0xffff0000, v91
	v_pk_add_f32 v[58:59], v[58:59], v[62:63]
	v_cvt_pk_bf16_f32 v57, v56, v57
	v_cvt_pk_bf16_f32 v56, v58, v59
	v_lshlrev_b32_e32 v58, 16, v92
	v_and_b32_e32 v59, 0xffff0000, v92
	v_pk_add_f32 v[52:53], v[52:53], v[58:59]
	v_lshlrev_b32_e32 v58, 16, v93
	v_and_b32_e32 v59, 0xffff0000, v93
	v_pk_add_f32 v[54:55], v[54:55], v[58:59]
	v_cvt_pk_bf16_f32 v53, v52, v53
	v_cvt_pk_bf16_f32 v52, v54, v55
	v_lshlrev_b32_e32 v54, 16, v94
	v_and_b32_e32 v55, 0xffff0000, v94
	v_pk_add_f32 v[48:49], v[48:49], v[54:55]
	v_lshlrev_b32_e32 v54, 16, v95
	v_and_b32_e32 v55, 0xffff0000, v95
	v_pk_add_f32 v[50:51], v[50:51], v[54:55]
	v_cvt_pk_bf16_f32 v49, v48, v49
	v_cvt_pk_bf16_f32 v48, v50, v51
	v_cndmask_b32_e64 v50, v56, v48, s[4:5]
	v_cndmask_b32_e64 v51, v60, v52, s[4:5]
	v_cndmask_b32_e64 v54, v57, v49, s[4:5]
	v_cndmask_b32_e64 v55, v61, v53, s[4:5]
	ds_bpermute_b32 v55, v178, v55
	ds_bpermute_b32 v58, v178, v51
	ds_bpermute_b32 v54, v178, v54
	ds_bpermute_b32 v59, v178, v50
	v_lshl_add_u64 v[50:51], s[36:37], 0, v[208:209]
	v_lshl_add_u64 v[50:51], v[50:51], 0, v[112:113]
	v_lshl_add_u64 v[50:51], v[50:51], 0, v[114:115]
	s_waitcnt lgkmcnt(2)
	v_cndmask_b32_e64 v89, v58, v60, s[4:5]
	s_waitcnt lgkmcnt(0)
	v_cndmask_b32_e64 v91, v59, v56, s[4:5]
	v_cndmask_b32_e64 v90, v54, v57, s[4:5]
	v_cndmask_b32_e64 v88, v55, v61, s[4:5]
	global_store_dwordx4 v[50:51], v[88:91], off nt
	v_add_co_u32_e32 v50, vcc, s23, v50
	s_nop 0
	v_cndmask_b32_e64 v91, v48, v59, s[4:5]
	v_cndmask_b32_e64 v89, v52, v58, s[4:5]
	v_cndmask_b32_e64 v90, v49, v54, s[4:5]
	v_cndmask_b32_e64 v88, v53, v55, s[4:5]
	v_addc_co_u32_e32 v51, vcc, 0, v51, vcc
	global_store_dwordx4 v[50:51], v[88:91], off nt
	v_and_b32_e32 v51, 0xffff0000, v61
	v_lshlrev_b32_e32 v50, 16, v61
	v_mul_f32_e32 v51, v51, v51
	v_and_b32_e32 v54, 0xffff0000, v60
	v_fmac_f32_e32 v51, v50, v50
	v_lshlrev_b32_e32 v50, 16, v60
	v_mul_f32_e32 v54, v54, v54
	v_fmac_f32_e32 v54, v50, v50
	v_add_f32_e32 v50, v51, v54
	v_and_b32_e32 v54, 0xffff0000, v57
	v_lshlrev_b32_e32 v51, 16, v57
	v_mul_f32_e32 v54, v54, v54
	v_fmac_f32_e32 v54, v51, v51
	v_add_f32_e32 v50, v54, v50
	v_and_b32_e32 v54, 0xffff0000, v56
	v_lshlrev_b32_e32 v51, 16, v56
	v_mul_f32_e32 v54, v54, v54
	v_fmac_f32_e32 v54, v51, v51
	v_lshlrev_b32_e32 v51, 16, v53
	v_and_b32_e32 v53, 0xffff0000, v53
	v_mul_f32_e32 v53, v53, v53
	v_fmac_f32_e32 v53, v51, v51
	v_lshlrev_b32_e32 v51, 16, v52
	v_and_b32_e32 v52, 0xffff0000, v52
	v_mul_f32_e32 v52, v52, v52
	v_fmac_f32_e32 v52, v51, v51
	v_add_f32_e32 v51, v53, v52
	v_lshlrev_b32_e32 v52, 16, v49
	v_and_b32_e32 v49, 0xffff0000, v49
	v_mul_f32_e32 v49, v49, v49
	v_fmac_f32_e32 v49, v52, v52
	v_add_f32_e32 v49, v49, v51
	v_lshlrev_b32_e32 v51, 16, v48
	v_and_b32_e32 v48, 0xffff0000, v48
	v_mul_f32_e32 v48, v48, v48
	v_fmac_f32_e32 v48, v51, v51
	v_add_f32_e32 v50, v54, v50
	v_add_f32_e32 v48, v48, v49
	v_add_f32_e32 v48, v50, v48
	ds_bpermute_b32 v49, v176, v48
	s_waitcnt lgkmcnt(0)
	v_add_f32_e32 v48, v48, v49
	ds_bpermute_b32 v49, v177, v48
	s_and_saveexec_b64 s[36:37], s[6:7]
	s_cbranch_execz .LBB0_1349
	s_waitcnt lgkmcnt(0)
	v_add_f32_e32 v50, v48, v49
	v_or_b32_e32 v48, s34, v165
	v_ashrrev_i32_e32 v49, 31, v48
	v_lshlrev_b64 v[48:49], 6, v[48:49]
	v_lshl_add_u64 v[48:49], s[16:17], 0, v[48:49]
	v_lshl_add_u64 v[48:49], s[26:27], 2, v[48:49]
	s_lshl_b32 s68, s58, 2
	v_lshl_add_u64 v[48:49], v[48:49], 0, s[68:69]
	global_store_dword v[48:49], v50, off
.LBB0_1349:
	s_or_b64 exec, exec, s[36:37]
	v_lshlrev_b32_e32 v48, 16, v84
	s_waitcnt lgkmcnt(0)
	v_and_b32_e32 v49, 0xffff0000, v84
	v_pk_add_f32 v[44:45], v[44:45], v[48:49]
	s_add_i32 s34, s28, 0x90
	v_cvt_pk_bf16_f32 v48, v44, v45
	v_lshlrev_b32_e32 v44, 16, v85
	v_and_b32_e32 v45, 0xffff0000, v85
	v_pk_add_f32 v[44:45], v[46:47], v[44:45]
	s_ashr_i32 s35, s34, 31
	v_cvt_pk_bf16_f32 v46, v44, v45
	v_lshlrev_b32_e32 v44, 16, v86
	v_and_b32_e32 v45, 0xffff0000, v86
	v_pk_add_f32 v[40:41], v[40:41], v[44:45]
	s_lshl_b64 s[36:37], s[34:35], 11
	v_cvt_pk_bf16_f32 v44, v40, v41
	v_lshlrev_b32_e32 v40, 16, v87
	v_and_b32_e32 v41, 0xffff0000, v87
	v_pk_add_f32 v[40:41], v[42:43], v[40:41]
	s_add_u32 s23, s14, s36
	v_cvt_pk_bf16_f32 v42, v40, v41
	v_lshlrev_b32_e32 v40, 16, v80
	v_and_b32_e32 v41, 0xffff0000, v80
	v_pk_add_f32 v[36:37], v[36:37], v[40:41]
	s_addc_u32 s25, s15, s37
	v_cvt_pk_bf16_f32 v40, v36, v37
	v_lshlrev_b32_e32 v36, 16, v81
	v_and_b32_e32 v37, 0xffff0000, v81
	v_pk_add_f32 v[36:37], v[38:39], v[36:37]
	s_add_u32 s36, s23, s30
	v_cvt_pk_bf16_f32 v41, v36, v37
	v_lshlrev_b32_e32 v36, 16, v82
	v_and_b32_e32 v37, 0xffff0000, v82
	v_pk_add_f32 v[32:33], v[32:33], v[36:37]
	s_addc_u32 s37, s25, s31
	v_cvt_pk_bf16_f32 v36, v32, v33
	v_lshlrev_b32_e32 v32, 16, v83
	v_and_b32_e32 v33, 0xffff0000, v83
	v_pk_add_f32 v[32:33], v[34:35], v[32:33]
	v_cndmask_b32_e64 v34, v44, v36, s[4:5]
	v_cvt_pk_bf16_f32 v37, v32, v33
	v_cndmask_b32_e64 v32, v42, v37, s[4:5]
	v_cndmask_b32_e64 v33, v46, v41, s[4:5]
	v_cndmask_b32_e64 v35, v48, v40, s[4:5]
	ds_bpermute_b32 v43, v178, v35
	ds_bpermute_b32 v45, v178, v33
	ds_bpermute_b32 v47, v178, v32
	ds_bpermute_b32 v49, v178, v34
	v_lshl_add_u64 v[32:33], s[36:37], 0, v[208:209]
	v_lshl_add_u64 v[32:33], v[32:33], 0, v[112:113]
	v_lshl_add_u64 v[38:39], v[32:33], 0, v[114:115]
	s_waitcnt lgkmcnt(1)
	v_cndmask_b32_e64 v35, v47, v42, s[4:5]
	v_cndmask_b32_e64 v33, v45, v46, s[4:5]
	s_waitcnt lgkmcnt(0)
	v_cndmask_b32_e64 v34, v49, v44, s[4:5]
	v_cndmask_b32_e64 v32, v43, v48, s[4:5]
	global_store_dwordx4 v[38:39], v[32:35], off nt
	s_movk_i32 s23, 0x4000
	v_add_co_u32_e32 v38, vcc, s23, v38
	v_and_b32_e32 v33, 0xffff0000, v48
	v_lshlrev_b32_e32 v32, 16, v48
	v_mul_f32_e32 v33, v33, v33
	v_and_b32_e32 v34, 0xffff0000, v46
	v_fmac_f32_e32 v33, v32, v32
	v_lshlrev_b32_e32 v32, 16, v46
	v_mul_f32_e32 v34, v34, v34
	v_fmac_f32_e32 v34, v32, v32
	v_add_f32_e32 v32, v33, v34
	v_and_b32_e32 v34, 0xffff0000, v44
	v_lshlrev_b32_e32 v33, 16, v44
	v_mul_f32_e32 v34, v34, v34
	v_fmac_f32_e32 v34, v33, v33
	v_add_f32_e32 v32, v34, v32
	v_and_b32_e32 v34, 0xffff0000, v42
	v_lshlrev_b32_e32 v33, 16, v42
	v_mul_f32_e32 v34, v34, v34
	v_fmac_f32_e32 v34, v33, v33
	v_add_f32_e32 v32, v34, v32
	v_and_b32_e32 v34, 0xffff0000, v40
	v_lshlrev_b32_e32 v33, 16, v40
	v_mul_f32_e32 v34, v34, v34
	v_and_b32_e32 v35, 0xffff0000, v41
	v_fmac_f32_e32 v34, v33, v33
	v_lshlrev_b32_e32 v33, 16, v41
	v_mul_f32_e32 v35, v35, v35
	v_fmac_f32_e32 v35, v33, v33
	v_add_f32_e32 v33, v34, v35
	v_and_b32_e32 v35, 0xffff0000, v36
	v_lshlrev_b32_e32 v34, 16, v36
	v_mul_f32_e32 v35, v35, v35
	v_fmac_f32_e32 v35, v34, v34
	v_add_f32_e32 v33, v35, v33
	v_and_b32_e32 v35, 0xffff0000, v37
	v_lshlrev_b32_e32 v34, 16, v37
	v_mul_f32_e32 v35, v35, v35
	v_fmac_f32_e32 v35, v34, v34
	v_add_f32_e32 v33, v35, v33
	v_add_f32_e32 v32, v32, v33
	ds_bpermute_b32 v33, v176, v32
	v_cndmask_b32_e64 v37, v37, v47, s[4:5]
	v_cndmask_b32_e64 v35, v41, v45, s[4:5]
	v_cndmask_b32_e64 v36, v36, v49, s[4:5]
	v_cndmask_b32_e64 v34, v40, v43, s[4:5]
	s_waitcnt lgkmcnt(0)
	v_add_f32_e32 v32, v32, v33
	ds_bpermute_b32 v33, v177, v32
	v_addc_co_u32_e32 v39, vcc, 0, v39, vcc
	global_store_dwordx4 v[38:39], v[34:37], off nt
	s_and_saveexec_b64 s[36:37], s[6:7]
	s_cbranch_execz .LBB0_1351
	s_waitcnt lgkmcnt(0)
	v_add_f32_e32 v34, v32, v33
	v_or_b32_e32 v32, s34, v165
	v_ashrrev_i32_e32 v33, 31, v32
	v_lshlrev_b64 v[32:33], 6, v[32:33]
	v_lshl_add_u64 v[32:33], s[16:17], 0, v[32:33]
	v_lshl_add_u64 v[32:33], s[26:27], 2, v[32:33]
	s_lshl_b32 s68, s58, 2
	v_lshl_add_u64 v[32:33], v[32:33], 0, s[68:69]
	global_store_dword v[32:33], v34, off
.LBB0_1351:
	s_or_b64 exec, exec, s[36:37]
	v_lshlrev_b32_e32 v32, 16, v76
	s_waitcnt lgkmcnt(0)
	v_and_b32_e32 v33, 0xffff0000, v76
	v_pk_add_f32 v[28:29], v[28:29], v[32:33]
	s_add_i32 s34, s28, 0xa0
	v_cvt_pk_bf16_f32 v32, v28, v29
	v_lshlrev_b32_e32 v28, 16, v77
	v_and_b32_e32 v29, 0xffff0000, v77
	v_pk_add_f32 v[28:29], v[30:31], v[28:29]
	s_ashr_i32 s35, s34, 31
	v_cvt_pk_bf16_f32 v30, v28, v29
	v_lshlrev_b32_e32 v28, 16, v78
	v_and_b32_e32 v29, 0xffff0000, v78
	v_pk_add_f32 v[24:25], v[24:25], v[28:29]
	s_lshl_b64 s[36:37], s[34:35], 11
	v_cvt_pk_bf16_f32 v28, v24, v25
	v_lshlrev_b32_e32 v24, 16, v79
	v_and_b32_e32 v25, 0xffff0000, v79
	v_pk_add_f32 v[24:25], v[26:27], v[24:25]
	s_add_u32 s23, s14, s36
	v_cvt_pk_bf16_f32 v26, v24, v25
	v_lshlrev_b32_e32 v24, 16, v72
	v_and_b32_e32 v25, 0xffff0000, v72
	v_pk_add_f32 v[20:21], v[20:21], v[24:25]
	s_addc_u32 s25, s15, s37
	v_cvt_pk_bf16_f32 v24, v20, v21
	v_lshlrev_b32_e32 v20, 16, v73
	v_and_b32_e32 v21, 0xffff0000, v73
	v_pk_add_f32 v[20:21], v[22:23], v[20:21]
	s_add_u32 s36, s23, s30
	v_cvt_pk_bf16_f32 v25, v20, v21
	v_lshlrev_b32_e32 v20, 16, v74
	v_and_b32_e32 v21, 0xffff0000, v74
	v_pk_add_f32 v[16:17], v[16:17], v[20:21]
	s_addc_u32 s37, s25, s31
	v_cvt_pk_bf16_f32 v20, v16, v17
	v_lshlrev_b32_e32 v16, 16, v75
	v_and_b32_e32 v17, 0xffff0000, v75
	v_pk_add_f32 v[16:17], v[18:19], v[16:17]
	v_cndmask_b32_e64 v18, v28, v20, s[4:5]
	v_cvt_pk_bf16_f32 v21, v16, v17
	v_cndmask_b32_e64 v16, v26, v21, s[4:5]
	v_cndmask_b32_e64 v17, v30, v25, s[4:5]
	v_cndmask_b32_e64 v19, v32, v24, s[4:5]
	ds_bpermute_b32 v27, v178, v19
	ds_bpermute_b32 v29, v178, v17
	ds_bpermute_b32 v31, v178, v18
	ds_bpermute_b32 v33, v178, v16
	v_lshl_add_u64 v[16:17], s[36:37], 0, v[208:209]
	v_mov_b32_e32 v113, v209
	v_lshl_add_u64 v[16:17], v[16:17], 0, v[112:113]
	v_mov_b32_e32 v115, v209
	v_lshl_add_u64 v[22:23], v[16:17], 0, v[114:115]
	s_waitcnt lgkmcnt(0)
	v_cndmask_b32_e64 v19, v33, v26, s[4:5]
	v_cndmask_b32_e64 v17, v29, v30, s[4:5]
	v_cndmask_b32_e64 v18, v31, v28, s[4:5]
	v_cndmask_b32_e64 v16, v27, v32, s[4:5]
	global_store_dwordx4 v[22:23], v[16:19], off nt
	s_movk_i32 s23, 0x4000
	v_add_co_u32_e32 v22, vcc, s23, v22
	v_and_b32_e32 v17, 0xffff0000, v32
	v_lshlrev_b32_e32 v16, 16, v32
	v_mul_f32_e32 v17, v17, v17
	v_and_b32_e32 v18, 0xffff0000, v30
	v_fmac_f32_e32 v17, v16, v16
	v_lshlrev_b32_e32 v16, 16, v30
	v_mul_f32_e32 v18, v18, v18
	v_fmac_f32_e32 v18, v16, v16
	v_add_f32_e32 v16, v17, v18
	v_and_b32_e32 v18, 0xffff0000, v28
	v_lshlrev_b32_e32 v17, 16, v28
	v_mul_f32_e32 v18, v18, v18
	v_fmac_f32_e32 v18, v17, v17
	v_add_f32_e32 v16, v18, v16
	v_and_b32_e32 v18, 0xffff0000, v26
	v_lshlrev_b32_e32 v17, 16, v26
	v_mul_f32_e32 v18, v18, v18
	v_fmac_f32_e32 v18, v17, v17
	v_add_f32_e32 v16, v18, v16
	v_and_b32_e32 v18, 0xffff0000, v24
	v_lshlrev_b32_e32 v17, 16, v24
	v_mul_f32_e32 v18, v18, v18
	v_and_b32_e32 v19, 0xffff0000, v25
	v_fmac_f32_e32 v18, v17, v17
	v_lshlrev_b32_e32 v17, 16, v25
	v_mul_f32_e32 v19, v19, v19
	v_fmac_f32_e32 v19, v17, v17
	v_add_f32_e32 v17, v18, v19
	v_and_b32_e32 v19, 0xffff0000, v20
	v_lshlrev_b32_e32 v18, 16, v20
	v_mul_f32_e32 v19, v19, v19
	v_fmac_f32_e32 v19, v18, v18
	v_add_f32_e32 v17, v19, v17
	v_and_b32_e32 v19, 0xffff0000, v21
	v_lshlrev_b32_e32 v18, 16, v21
	v_mul_f32_e32 v19, v19, v19
	v_fmac_f32_e32 v19, v18, v18
	v_add_f32_e32 v17, v19, v17
	v_add_f32_e32 v16, v16, v17
	ds_bpermute_b32 v17, v176, v16
	v_cndmask_b32_e64 v21, v21, v33, s[4:5]
	v_cndmask_b32_e64 v19, v25, v29, s[4:5]
	v_cndmask_b32_e64 v20, v20, v31, s[4:5]
	v_cndmask_b32_e64 v18, v24, v27, s[4:5]
	s_waitcnt lgkmcnt(0)
	v_add_f32_e32 v16, v16, v17
	ds_bpermute_b32 v17, v177, v16
	v_addc_co_u32_e32 v23, vcc, 0, v23, vcc
	global_store_dwordx4 v[22:23], v[18:21], off nt
	s_and_saveexec_b64 s[36:37], s[6:7]
	s_cbranch_execz .LBB0_1353
	s_waitcnt lgkmcnt(0)
	v_add_f32_e32 v18, v16, v17
	v_or_b32_e32 v16, s34, v165
	v_ashrrev_i32_e32 v17, 31, v16
	v_lshlrev_b64 v[16:17], 6, v[16:17]
	v_lshl_add_u64 v[16:17], s[16:17], 0, v[16:17]
	v_lshl_add_u64 v[16:17], s[26:27], 2, v[16:17]
	s_lshl_b32 s68, s58, 2
	v_lshl_add_u64 v[16:17], v[16:17], 0, s[68:69]
	global_store_dword v[16:17], v18, off
.LBB0_1353:
	s_or_b64 exec, exec, s[36:37]
	v_lshlrev_b32_e32 v16, 16, v68
	s_waitcnt lgkmcnt(0)
	v_and_b32_e32 v17, 0xffff0000, v68
	v_pk_add_f32 v[12:13], v[12:13], v[16:17]
	s_addk_i32 s28, 0xb0
	v_cvt_pk_bf16_f32 v16, v12, v13
	v_lshlrev_b32_e32 v12, 16, v69
	v_and_b32_e32 v13, 0xffff0000, v69
	v_pk_add_f32 v[12:13], v[14:15], v[12:13]
	s_ashr_i32 s29, s28, 31
	v_cvt_pk_bf16_f32 v14, v12, v13
	v_lshlrev_b32_e32 v12, 16, v70
	v_and_b32_e32 v13, 0xffff0000, v70
	v_pk_add_f32 v[8:9], v[8:9], v[12:13]
	s_lshl_b64 s[34:35], s[28:29], 11
	v_cvt_pk_bf16_f32 v12, v8, v9
	v_lshlrev_b32_e32 v8, 16, v71
	v_and_b32_e32 v9, 0xffff0000, v71
	v_pk_add_f32 v[8:9], v[10:11], v[8:9]
	s_add_u32 s23, s14, s34
	v_cvt_pk_bf16_f32 v10, v8, v9
	v_lshlrev_b32_e32 v8, 16, v64
	v_and_b32_e32 v9, 0xffff0000, v64
	v_pk_add_f32 v[4:5], v[4:5], v[8:9]
	s_addc_u32 s25, s15, s35
	v_cvt_pk_bf16_f32 v8, v4, v5
	v_lshlrev_b32_e32 v4, 16, v65
	v_and_b32_e32 v5, 0xffff0000, v65
	v_pk_add_f32 v[4:5], v[6:7], v[4:5]
	s_add_u32 s30, s23, s30
	v_cvt_pk_bf16_f32 v9, v4, v5
	v_lshlrev_b32_e32 v4, 16, v66
	v_and_b32_e32 v5, 0xffff0000, v66
	v_pk_add_f32 v[0:1], v[0:1], v[4:5]
	s_addc_u32 s31, s25, s31
	v_cvt_pk_bf16_f32 v4, v0, v1
	v_lshlrev_b32_e32 v0, 16, v67
	v_and_b32_e32 v1, 0xffff0000, v67
	v_pk_add_f32 v[0:1], v[2:3], v[0:1]
	v_cndmask_b32_e64 v2, v12, v4, s[4:5]
	v_cvt_pk_bf16_f32 v5, v0, v1
	v_cndmask_b32_e64 v0, v10, v5, s[4:5]
	v_cndmask_b32_e64 v1, v14, v9, s[4:5]
	v_cndmask_b32_e64 v3, v16, v8, s[4:5]
	ds_bpermute_b32 v11, v178, v3
	ds_bpermute_b32 v13, v178, v1
	ds_bpermute_b32 v15, v178, v0
	ds_bpermute_b32 v17, v178, v2
	v_lshl_add_u64 v[0:1], s[30:31], 0, v[208:209]
	v_lshl_add_u64 v[0:1], v[0:1], 0, v[112:113]
	v_lshl_add_u64 v[6:7], v[0:1], 0, v[114:115]
	s_waitcnt lgkmcnt(1)
	v_cndmask_b32_e64 v3, v15, v10, s[4:5]
	v_cndmask_b32_e64 v1, v13, v14, s[4:5]
	s_waitcnt lgkmcnt(0)
	v_cndmask_b32_e64 v2, v17, v12, s[4:5]
	v_cndmask_b32_e64 v0, v11, v16, s[4:5]
	global_store_dwordx4 v[6:7], v[0:3], off nt
	s_movk_i32 s23, 0x4000
	v_add_co_u32_e32 v6, vcc, s23, v6
	v_and_b32_e32 v1, 0xffff0000, v16
	v_lshlrev_b32_e32 v0, 16, v16
	v_mul_f32_e32 v1, v1, v1
	v_and_b32_e32 v2, 0xffff0000, v14
	v_fmac_f32_e32 v1, v0, v0
	v_lshlrev_b32_e32 v0, 16, v14
	v_mul_f32_e32 v2, v2, v2
	v_fmac_f32_e32 v2, v0, v0
	v_add_f32_e32 v0, v1, v2
	v_and_b32_e32 v2, 0xffff0000, v12
	v_lshlrev_b32_e32 v1, 16, v12
	v_mul_f32_e32 v2, v2, v2
	v_fmac_f32_e32 v2, v1, v1
	v_add_f32_e32 v0, v2, v0
	v_and_b32_e32 v2, 0xffff0000, v10
	v_lshlrev_b32_e32 v1, 16, v10
	v_mul_f32_e32 v2, v2, v2
	v_fmac_f32_e32 v2, v1, v1
	v_add_f32_e32 v0, v2, v0
	v_and_b32_e32 v2, 0xffff0000, v8
	v_lshlrev_b32_e32 v1, 16, v8
	v_mul_f32_e32 v2, v2, v2
	v_and_b32_e32 v3, 0xffff0000, v9
	v_fmac_f32_e32 v2, v1, v1
	v_lshlrev_b32_e32 v1, 16, v9
	v_mul_f32_e32 v3, v3, v3
	v_fmac_f32_e32 v3, v1, v1
	v_add_f32_e32 v1, v2, v3
	v_and_b32_e32 v3, 0xffff0000, v4
	v_lshlrev_b32_e32 v2, 16, v4
	v_mul_f32_e32 v3, v3, v3
	v_fmac_f32_e32 v3, v2, v2
	v_add_f32_e32 v1, v3, v1
	v_and_b32_e32 v3, 0xffff0000, v5
	v_lshlrev_b32_e32 v2, 16, v5
	v_mul_f32_e32 v3, v3, v3
	v_fmac_f32_e32 v3, v2, v2
	v_add_f32_e32 v1, v3, v1
	v_add_f32_e32 v0, v0, v1
	ds_bpermute_b32 v1, v176, v0
	v_cndmask_b32_e64 v5, v5, v15, s[4:5]
	v_cndmask_b32_e64 v3, v9, v13, s[4:5]
	v_cndmask_b32_e64 v4, v4, v17, s[4:5]
	v_cndmask_b32_e64 v2, v8, v11, s[4:5]
	s_waitcnt lgkmcnt(0)
	v_add_f32_e32 v0, v0, v1
	ds_bpermute_b32 v1, v177, v0
	v_addc_co_u32_e32 v7, vcc, 0, v7, vcc
	global_store_dwordx4 v[6:7], v[2:5], off nt
	s_and_saveexec_b64 s[30:31], s[6:7]
	s_cbranch_execz .LBB0_1355
	s_waitcnt lgkmcnt(0)
	v_add_f32_e32 v2, v0, v1
	v_or_b32_e32 v0, s28, v165
	v_ashrrev_i32_e32 v1, 31, v0
	v_lshlrev_b64 v[0:1], 6, v[0:1]
	v_lshl_add_u64 v[0:1], s[16:17], 0, v[0:1]
	v_lshl_add_u64 v[0:1], s[26:27], 2, v[0:1]
	s_lshl_b32 s68, s58, 2
	v_lshl_add_u64 v[0:1], v[0:1], 0, s[68:69]
	global_store_dword v[0:1], v2, off
